# MoE: next-unit token gathers (P7) and the Y2-scatter epilogue's index/weight loads (P8) requested together and awaited once
# speedup vs baseline: 1.0074x; 1.0074x over previous
; #define MG_STAGE_A(b, rows, k0) do { _Pragma("unroll") for (int h_ = 0; h_ < 2; ++h_) _Pragma("unroll") for (int i_ = 0; i_ < 2; ++i_) if (rows[h_][i_] != 0xffffffffu) \
;         __builtin_amdgcn_global_load_lds((const unsigned*)((const char*)Abase + rows[h_][i_] + (k0) * 2), (PG8_LAS unsigned*)(lds + MG_SA(b, h_) + ldsw + i_ * 8192), 16, 0, 0); } while (0)
; template <class Epi, bool G1> ...
;     ...
;             else if (has_next) { MG_ROWS(nxt, rowC); MG_STAGE_A(buf ^ 1, rowC, 0); }
.LBB0_1122:
	s_lshl_b32 s15, s14, 2
	s_add_i32 s15, s15, 0
	s_add_i32 s38, s15, 0x20200
	s_add_i32 s15, s15, 0x20000
	v_mov_b32_e32 v192, s15
	v_mov_b32_e32 v193, s38
	ds_read_b32 v192, v192
	ds_read_b32 v193, v193
	s_lshl_b32 s38, s65, 8
	s_lshl_b32 s14, s14, 14
	v_mov_b32_e32 v194, -1
	s_waitcnt lgkmcnt(0)
	v_sub_u32_e32 v195, s14, v192
	v_add_u32_e32 v196, v193, v192
	v_mov_b32_e32 v192, -1
	v_mov_b32_e32 v198, -1
	v_mov_b32_e32 v193, -1
	v_add_u32_e32 v206, s38, v214
	v_add_u32_e32 v207, s38, v215
	s_bitset1_b32 s38, 7
	v_add_u32_e32 v208, s38, v214
	v_add_u32_e32 v209, s38, v215
	v_cmp_lt_i32_e32 vcc, v206, v196
	s_and_saveexec_b64 s[14:15], vcc
	v_add_u32_e32 v210, v195, v206
	v_ashrrev_i32_e32 v211, 31, v210
	v_lshl_add_u64 v[210:211], v[210:211], 2, s[16:17]
	global_load_dword v194, v[210:211], off
	s_or_b64 exec, exec, s[14:15]
	v_cmp_lt_i32_e32 vcc, v207, v196
	s_and_saveexec_b64 s[14:15], vcc
	v_add_u32_e32 v212, v195, v207
	v_ashrrev_i32_e32 v213, 31, v212
	v_lshl_add_u64 v[212:213], v[212:213], 2, s[16:17]
	global_load_dword v192, v[212:213], off
	s_or_b64 exec, exec, s[14:15]
	v_cmp_lt_i32_e32 vcc, v208, v196
	s_and_saveexec_b64 s[14:15], vcc
	v_add_u32_e32 v226, v195, v208
	v_ashrrev_i32_e32 v227, 31, v226
	v_lshl_add_u64 v[226:227], v[226:227], 2, s[16:17]
	global_load_dword v198, v[226:227], off
	s_or_b64 exec, exec, s[14:15]
	v_cmp_lt_i32_e32 vcc, v209, v196
	s_and_saveexec_b64 s[14:15], vcc
	v_add_u32_e32 v228, v195, v209
	v_ashrrev_i32_e32 v229, 31, v228
	v_lshl_add_u64 v[228:229], v[228:229], 2, s[16:17]
	global_load_dword v193, v[228:229], off
	s_or_b64 exec, exec, s[14:15]
	s_waitcnt vmcnt(0)
	v_cmp_ne_u32_e32 vcc, -1, v194
	v_lshlrev_b32_e32 v206, 11, v194
	v_and_b32_e32 v206, 0xfffff000, v206
	v_add_u32_e32 v206, v206, v223
	v_cndmask_b32_e32 v194, v194, v206, vcc
	v_cmp_ne_u32_e32 vcc, -1, v192
	v_lshlrev_b32_e32 v206, 11, v192
	v_and_b32_e32 v206, 0xfffff000, v206
	v_add_u32_e32 v206, v206, v224
	v_cndmask_b32_e32 v192, v192, v206, vcc
	v_cmp_ne_u32_e32 vcc, -1, v198
	v_lshlrev_b32_e32 v206, 11, v198
	v_and_b32_e32 v206, 0xfffff000, v206
	v_add_u32_e32 v206, v206, v223
	v_cndmask_b32_e32 v198, v198, v206, vcc
	v_cmp_ne_u32_e32 vcc, -1, v193
	v_lshlrev_b32_e32 v206, 11, v193
	v_and_b32_e32 v206, 0xfffff000, v206
	v_add_u32_e32 v206, v206, v224
	v_cndmask_b32_e32 v193, v193, v206, vcc
	s_mov_b64 s[14:15], exec
	s_or_b64 exec, exec, s[14:15]
	v_cmp_ne_u32_e32 vcc, -1, v194
	s_and_saveexec_b64 s[14:15], vcc
	s_cbranch_execnz .LBB0_1145

; template <class Epi, bool G1> ...
;     ...
; #pragma unroll
;         for (int a = 0; a < 2; ++a)
; #pragma unroll
;             for (int b = 0; b < 2; ++b)
; #pragma unroll
;                 for (int m = 0; m < 4; ++m)
; #pragma unroll
;                     for (int n = 0; n < 2; ++n) acc[a][b][m][n] = (f32x4){0.f, 0.f, 0.f, 0.f};
;         cur = nxt; ++ui;
.LBB0_1143:
	v_mov_b32_e32 v26, v197
	v_mov_b32_e32 v27, v197
	v_mov_b32_e32 v24, v197
	v_mov_b32_e32 v25, v197
	v_mov_b64_e32 v[34:35], v[26:27]
	v_mov_b64_e32 v[38:39], v[26:27]
	v_mov_b64_e32 v[42:43], v[26:27]
	v_mov_b64_e32 v[50:51], v[26:27]
	v_mov_b64_e32 v[54:55], v[26:27]
	v_mov_b64_e32 v[58:59], v[26:27]
	v_mov_b64_e32 v[62:63], v[26:27]
	v_mov_b64_e32 v[66:67], v[26:27]
	v_mov_b64_e32 v[70:71], v[26:27]
	v_mov_b64_e32 v[74:75], v[26:27]
	v_mov_b64_e32 v[78:79], v[26:27]
	v_mov_b64_e32 v[82:83], v[26:27]
	v_mov_b64_e32 v[86:87], v[26:27]
	v_mov_b64_e32 v[90:91], v[26:27]
	v_mov_b64_e32 v[94:95], v[26:27]
	v_mov_b64_e32 v[98:99], v[26:27]
	v_mov_b64_e32 v[102:103], v[26:27]
	v_mov_b64_e32 v[106:107], v[26:27]
	v_mov_b64_e32 v[110:111], v[26:27]
	v_mov_b64_e32 v[118:119], v[26:27]
	v_mov_b64_e32 v[126:127], v[26:27]
	v_mov_b64_e32 v[134:135], v[26:27]
	v_mov_b64_e32 v[142:143], v[26:27]
	v_mov_b64_e32 v[146:147], v[26:27]
	v_mov_b64_e32 v[150:151], v[26:27]
	v_mov_b64_e32 v[154:155], v[26:27]
	v_mov_b64_e32 v[158:159], v[26:27]
	v_mov_b64_e32 v[162:163], v[26:27]
	v_mov_b64_e32 v[166:167], v[26:27]
	v_mov_b64_e32 v[174:175], v[26:27]
	v_mov_b64_e32 v[182:183], v[26:27]
	v_mov_b64_e32 v[32:33], v[24:25]
	v_mov_b64_e32 v[36:37], v[24:25]
	v_mov_b64_e32 v[40:41], v[24:25]
	v_mov_b64_e32 v[48:49], v[24:25]
	v_mov_b64_e32 v[52:53], v[24:25]
	v_mov_b64_e32 v[56:57], v[24:25]
	v_mov_b64_e32 v[60:61], v[24:25]
	v_mov_b64_e32 v[64:65], v[24:25]
	v_mov_b64_e32 v[68:69], v[24:25]
	v_mov_b64_e32 v[72:73], v[24:25]
	v_mov_b64_e32 v[76:77], v[24:25]
	v_mov_b64_e32 v[80:81], v[24:25]
	v_mov_b64_e32 v[84:85], v[24:25]
	v_mov_b64_e32 v[88:89], v[24:25]
	v_mov_b64_e32 v[92:93], v[24:25]
	v_mov_b64_e32 v[96:97], v[24:25]
	v_mov_b64_e32 v[100:101], v[24:25]
	v_mov_b64_e32 v[104:105], v[24:25]
	v_mov_b64_e32 v[108:109], v[24:25]
	v_mov_b64_e32 v[116:117], v[24:25]
	v_mov_b64_e32 v[124:125], v[24:25]
	v_mov_b64_e32 v[132:133], v[24:25]
	v_mov_b64_e32 v[140:141], v[24:25]
	v_mov_b64_e32 v[144:145], v[24:25]
	v_mov_b64_e32 v[148:149], v[24:25]
	v_mov_b64_e32 v[152:153], v[24:25]
	v_mov_b64_e32 v[156:157], v[24:25]
	v_mov_b64_e32 v[160:161], v[24:25]
	v_mov_b64_e32 v[164:165], v[24:25]
	v_mov_b64_e32 v[172:173], v[24:25]
	v_mov_b64_e32 v[180:181], v[24:25]
	s_mov_b32 s48, s69
	s_mov_b32 s50, s66
	s_mov_b32 s49, s65
	s_mov_b32 s67, s68
	s_branch .LBB0_1057
.LBB0_1145:
	s_add_i32 m0, s51, s72
	s_nop 0
	global_load_lds_dwordx4 v194, s[18:19]
	s_or_b64 exec, exec, s[14:15]
	v_cmp_ne_u32_e32 vcc, -1, v192
	s_and_saveexec_b64 s[14:15], vcc
	s_cbranch_execz .LBB0_1131

; __device__ __forceinline__ unsigned cvt_pk_bf16(float lo, float hi) { unsigned r; asm volatile("v_cvt_pk_bf16_f32 %0, %1, %2" : "=v"(r) : "v"(lo), "v"(hi)); return r; }
;     template <class Tp> __device__ __forceinline__ Tp* w(size_t off) const { return (Tp*)(ws + off); }
;     __device__ __forceinline__ void operator()(const f32x4 (&acc)[2][2][4][2], const Unit& u, int wr, int wc, int fr, int fq) const {
;         const int e = u.pn >> 3, lim = offs[e] + cnts[e], lb = e * 16384 - offs[e];
;         const int row0 = u.pm * BM + wr * 64 + fr, col0 = (u.pn & 7) * BM + wc * 32 + 8 * fq;
; #pragma unroll
;         for (int ai = 0; ai < 2; ++ai)
; #pragma unroll
;             for (int m = 0; m < 4; ++m) { const int p = row0 + ai * HALF + m * 16;
;                 if (p < lim) { const float w = wrow[lb + p]; bf16_t* rowp = Y2 + (size_t)tsi[lb + p] * 2048 + col0;
; #pragma unroll
;                     for (int bj = 0; bj < 2; ++bj) { const f32x4 v0 = acc[ai][bj][m][0] * w, v1 = acc[ai][bj][m][1] * w;
;                         u32x4 o; o.x = cvt_pk_bf16(v0[0], v0[1]); o.y = cvt_pk_bf16(v0[2], v0[3]); o.z = cvt_pk_bf16(v1[0], v1[1]); o.w = cvt_pk_bf16(v1[2], v1[3]);
;                         *(u32x4*)(rowp + bj * HALF) = o; } } }
;     }
.LBB0_1326:
	s_ashr_i32 s10, s56, 3
	s_lshl_b32 s11, s10, 2
	s_add_i32 s11, s11, 0
	s_add_i32 s12, s11, 0x20000
	s_add_i32 s11, s11, 0x20200
	v_mov_b32_e32 v2, s12
	v_mov_b32_e32 v3, s11
	ds_read_b32 v2, v2
	ds_read_b32 v3, v3
	s_lshl_b32 s10, s10, 14
	v_lshl_add_u32 v203, s55, 8, v219
	s_waitcnt lgkmcnt(0)
	v_sub_u32_e32 v199, s10, v2
	s_lshl_b32 s10, s56, 8
	s_and_b32 s10, s10, 0x700
	v_add_u32_e32 v201, v3, v2
	v_or_b32_e32 v2, s10, v224
	v_add_u32_e32 v208, 0, v203
	v_cmp_lt_i32_e32 vcc, v208, v201
	s_and_saveexec_b64 s[10:11], vcc
	v_add_u32_e32 v208, v199, v208
	v_ashrrev_i32_e32 v209, 31, v208
	v_lshlrev_b64 v[208:209], 2, v[208:209]
	v_lshl_add_u64 v[210:211], s[30:31], 0, v[208:209]
	v_lshl_add_u64 v[208:209], s[28:29], 0, v[208:209]
	global_load_dword v116, v[208:209], off
	global_load_dword v132, v[210:211], off
	s_or_b64 exec, exec, s[10:11]
	v_add_u32_e32 v208, 16, v203
	v_cmp_lt_i32_e32 vcc, v208, v201
	s_and_saveexec_b64 s[10:11], vcc
	v_add_u32_e32 v208, v199, v208
	v_ashrrev_i32_e32 v209, 31, v208
	v_lshlrev_b64 v[208:209], 2, v[208:209]
	v_lshl_add_u64 v[210:211], s[30:31], 0, v[208:209]
	v_lshl_add_u64 v[208:209], s[28:29], 0, v[208:209]
	global_load_dword v117, v[208:209], off
	global_load_dword v133, v[210:211], off
	s_or_b64 exec, exec, s[10:11]
	v_add_u32_e32 v208, 32, v203
	v_cmp_lt_i32_e32 vcc, v208, v201
	s_and_saveexec_b64 s[10:11], vcc
	v_add_u32_e32 v208, v199, v208
	v_ashrrev_i32_e32 v209, 31, v208
	v_lshlrev_b64 v[208:209], 2, v[208:209]
	v_lshl_add_u64 v[210:211], s[30:31], 0, v[208:209]
	v_lshl_add_u64 v[208:209], s[28:29], 0, v[208:209]
	global_load_dword v118, v[208:209], off
	global_load_dword v134, v[210:211], off
	s_or_b64 exec, exec, s[10:11]
	v_add_u32_e32 v208, 48, v203
	v_cmp_lt_i32_e32 vcc, v208, v201
	s_and_saveexec_b64 s[10:11], vcc
	v_add_u32_e32 v208, v199, v208
	v_ashrrev_i32_e32 v209, 31, v208
	v_lshlrev_b64 v[208:209], 2, v[208:209]
	v_lshl_add_u64 v[210:211], s[30:31], 0, v[208:209]
	v_lshl_add_u64 v[208:209], s[28:29], 0, v[208:209]
	global_load_dword v119, v[208:209], off
	global_load_dword v135, v[210:211], off
	s_or_b64 exec, exec, s[10:11]
	v_add_u32_e32 v208, 0x80, v203
	v_cmp_lt_i32_e32 vcc, v208, v201
	s_and_saveexec_b64 s[10:11], vcc
	v_add_u32_e32 v208, v199, v208
	v_ashrrev_i32_e32 v209, 31, v208
	v_lshlrev_b64 v[208:209], 2, v[208:209]
	v_lshl_add_u64 v[210:211], s[30:31], 0, v[208:209]
	v_lshl_add_u64 v[208:209], s[28:29], 0, v[208:209]
	global_load_dword v124, v[208:209], off
	global_load_dword v140, v[210:211], off
	s_or_b64 exec, exec, s[10:11]
	v_add_u32_e32 v208, 0x90, v203
	v_cmp_lt_i32_e32 vcc, v208, v201
	s_and_saveexec_b64 s[10:11], vcc
	v_add_u32_e32 v208, v199, v208
	v_ashrrev_i32_e32 v209, 31, v208
	v_lshlrev_b64 v[208:209], 2, v[208:209]
	v_lshl_add_u64 v[210:211], s[30:31], 0, v[208:209]
	v_lshl_add_u64 v[208:209], s[28:29], 0, v[208:209]
	global_load_dword v125, v[208:209], off
	global_load_dword v141, v[210:211], off
	s_or_b64 exec, exec, s[10:11]
	v_add_u32_e32 v208, 0xa0, v203
	v_cmp_lt_i32_e32 vcc, v208, v201
	s_and_saveexec_b64 s[10:11], vcc
	v_add_u32_e32 v208, v199, v208
	v_ashrrev_i32_e32 v209, 31, v208
	v_lshlrev_b64 v[208:209], 2, v[208:209]
	v_lshl_add_u64 v[210:211], s[30:31], 0, v[208:209]
	v_lshl_add_u64 v[208:209], s[28:29], 0, v[208:209]
	global_load_dword v126, v[208:209], off
	global_load_dword v142, v[210:211], off
	s_or_b64 exec, exec, s[10:11]
	v_add_u32_e32 v208, 0xb0, v203
	v_cmp_lt_i32_e32 vcc, v208, v201
	s_and_saveexec_b64 s[10:11], vcc
	v_add_u32_e32 v208, v199, v208
	v_ashrrev_i32_e32 v209, 31, v208
	v_lshlrev_b64 v[208:209], 2, v[208:209]
	v_lshl_add_u64 v[210:211], s[30:31], 0, v[208:209]
	v_lshl_add_u64 v[208:209], s[28:29], 0, v[208:209]
	global_load_dword v127, v[208:209], off
	global_load_dword v143, v[210:211], off
	s_or_b64 exec, exec, s[10:11]
	s_waitcnt vmcnt(0)
	v_cmp_lt_i32_e32 vcc, v203, v201
	v_lshlrev_b32_e32 v2, 1, v2
	s_and_saveexec_b64 s[10:11], vcc
	s_cbranch_execz .LBB0_1328
	v_mov_b32_e32 v208, v116
	v_mov_b32_e32 v210, v132
	v_mov_b32_e32 v3, v1
	v_ashrrev_i32_e32 v209, 31, v208
	v_pk_mul_f32 v[212:213], v[186:187], v[210:211] op_sel_hi:[1,0]
	v_lshlrev_b64 v[240:241], 12, v[208:209]
	v_pk_mul_f32 v[226:227], v[184:185], v[210:211] op_sel_hi:[1,0]
	v_pk_mul_f32 v[228:229], v[178:179], v[210:211] op_sel_hi:[1,0]
	v_cvt_pk_bf16_f32 v208, v226, v227
	v_cvt_pk_bf16_f32 v209, v212, v213
	v_lshl_add_u64 v[212:213], s[26:27], 0, v[240:241]
	v_pk_mul_f32 v[230:231], v[176:177], v[210:211] op_sel_hi:[1,0]
	v_pk_mul_f32 v[232:233], v[146:147], v[210:211] op_sel_hi:[1,0]
	v_pk_mul_f32 v[234:235], v[144:145], v[210:211] op_sel_hi:[1,0]
	v_pk_mul_f32 v[236:237], v[138:139], v[210:211] op_sel_hi:[1,0]
	v_pk_mul_f32 v[238:239], v[136:137], v[210:211] op_sel_hi:[1,0]
	v_cvt_pk_bf16_f32 v210, v230, v231
	v_cvt_pk_bf16_f32 v211, v228, v229
	v_lshl_add_u64 v[212:213], v[212:213], 0, v[2:3]
	global_store_dwordx4 v[212:213], v[208:211], off sc1
	s_nop 1
	v_cvt_pk_bf16_f32 v208, v234, v235
	v_cvt_pk_bf16_f32 v209, v232, v233
	v_cvt_pk_bf16_f32 v210, v238, v239
	v_cvt_pk_bf16_f32 v211, v236, v237
	global_store_dwordx4 v[212:213], v[208:211], off offset:256 sc1
; __device__ __forceinline__ unsigned cvt_pk_bf16(float lo, float hi) { unsigned r; asm volatile("v_cvt_pk_bf16_f32 %0, %1, %2" : "=v"(r) : "v"(lo), "v"(hi)); return r; }
;     template <class Tp> __device__ __forceinline__ Tp* w(size_t off) const { return (Tp*)(ws + off); }
;     __device__ __forceinline__ void operator()(const f32x4 (&acc)[2][2][4][2], const Unit& u, int wr, int wc, int fr, int fq) const {
;     ...
;             for (int m = 0; m < 4; ++m) { const int p = row0 + ai * HALF + m * 16;
;                 if (p < lim) { const float w = wrow[lb + p]; bf16_t* rowp = Y2 + (size_t)tsi[lb + p] * 2048 + col0;
; #pragma unroll
;                     for (int bj = 0; bj < 2; ++bj) { const f32x4 v0 = acc[ai][bj][m][0] * w, v1 = acc[ai][bj][m][1] * w;
;                         u32x4 o; o.x = cvt_pk_bf16(v0[0], v0[1]); o.y = cvt_pk_bf16(v0[2], v0[3]); o.z = cvt_pk_bf16(v1[0], v1[1]); o.w = cvt_pk_bf16(v1[2], v1[3]);
;                         *(u32x4*)(rowp + bj * HALF) = o; } } }
.LBB0_1328:
	s_or_b64 exec, exec, s[10:11]
	v_or_b32_e32 v3, 16, v203
	v_cmp_lt_i32_e32 vcc, v3, v201
	s_and_saveexec_b64 s[10:11], vcc
	s_cbranch_execz .LBB0_1330
	v_mov_b32_e32 v208, v117
	v_mov_b32_e32 v210, v133
	v_mov_b32_e32 v3, v1
	v_ashrrev_i32_e32 v209, 31, v208
	v_pk_mul_f32 v[212:213], v[170:171], v[210:211] op_sel_hi:[1,0]
	v_lshlrev_b64 v[240:241], 12, v[208:209]
	v_pk_mul_f32 v[226:227], v[168:169], v[210:211] op_sel_hi:[1,0]
	v_pk_mul_f32 v[228:229], v[166:167], v[210:211] op_sel_hi:[1,0]
	v_cvt_pk_bf16_f32 v208, v226, v227
	v_cvt_pk_bf16_f32 v209, v212, v213
	v_lshl_add_u64 v[212:213], s[26:27], 0, v[240:241]
	v_pk_mul_f32 v[230:231], v[164:165], v[210:211] op_sel_hi:[1,0]
	v_pk_mul_f32 v[232:233], v[130:131], v[210:211] op_sel_hi:[1,0]
	v_pk_mul_f32 v[234:235], v[128:129], v[210:211] op_sel_hi:[1,0]
	v_pk_mul_f32 v[236:237], v[122:123], v[210:211] op_sel_hi:[1,0]
	v_pk_mul_f32 v[238:239], v[120:121], v[210:211] op_sel_hi:[1,0]
	v_cvt_pk_bf16_f32 v210, v230, v231
	v_cvt_pk_bf16_f32 v211, v228, v229
	v_lshl_add_u64 v[212:213], v[212:213], 0, v[2:3]
	global_store_dwordx4 v[212:213], v[208:211], off sc1
	s_nop 1
	v_cvt_pk_bf16_f32 v208, v234, v235
	v_cvt_pk_bf16_f32 v209, v232, v233
	v_cvt_pk_bf16_f32 v210, v238, v239
	v_cvt_pk_bf16_f32 v211, v236, v237
	global_store_dwordx4 v[212:213], v[208:211], off offset:256 sc1
.LBB0_1330:
	s_or_b64 exec, exec, s[10:11]
	v_or_b32_e32 v3, 32, v203
	v_cmp_lt_i32_e32 vcc, v3, v201
	s_and_saveexec_b64 s[10:11], vcc
	s_cbranch_execz .LBB0_1332
	v_mov_b32_e32 v208, v118
	v_mov_b32_e32 v210, v134
	v_mov_b32_e32 v3, v1
	v_ashrrev_i32_e32 v209, 31, v208
	v_pk_mul_f32 v[212:213], v[162:163], v[210:211] op_sel_hi:[1,0]
	v_lshlrev_b64 v[240:241], 12, v[208:209]
	v_pk_mul_f32 v[226:227], v[160:161], v[210:211] op_sel_hi:[1,0]
	v_pk_mul_f32 v[228:229], v[158:159], v[210:211] op_sel_hi:[1,0]
	v_cvt_pk_bf16_f32 v208, v226, v227
	v_cvt_pk_bf16_f32 v209, v212, v213
	v_lshl_add_u64 v[212:213], s[26:27], 0, v[240:241]
	v_pk_mul_f32 v[230:231], v[156:157], v[210:211] op_sel_hi:[1,0]
	v_pk_mul_f32 v[232:233], v[114:115], v[210:211] op_sel_hi:[1,0]
	v_pk_mul_f32 v[234:235], v[112:113], v[210:211] op_sel_hi:[1,0]
	v_pk_mul_f32 v[236:237], v[110:111], v[210:211] op_sel_hi:[1,0]
	v_pk_mul_f32 v[238:239], v[108:109], v[210:211] op_sel_hi:[1,0]
	v_cvt_pk_bf16_f32 v210, v230, v231
	v_cvt_pk_bf16_f32 v211, v228, v229
	v_lshl_add_u64 v[212:213], v[212:213], 0, v[2:3]
	global_store_dwordx4 v[212:213], v[208:211], off sc1
	s_nop 1
	v_cvt_pk_bf16_f32 v208, v234, v235
	v_cvt_pk_bf16_f32 v209, v232, v233
	v_cvt_pk_bf16_f32 v210, v238, v239
	v_cvt_pk_bf16_f32 v211, v236, v237
	global_store_dwordx4 v[212:213], v[208:211], off offset:256 sc1
.LBB0_1332:
	s_or_b64 exec, exec, s[10:11]
	v_or_b32_e32 v3, 48, v203
	v_cmp_lt_i32_e32 vcc, v3, v201
	s_and_saveexec_b64 s[10:11], vcc
	s_cbranch_execz .LBB0_1334
	v_mov_b32_e32 v208, v119
	v_mov_b32_e32 v210, v135
	v_mov_b32_e32 v3, v1
	v_ashrrev_i32_e32 v209, 31, v208
	v_pk_mul_f32 v[212:213], v[154:155], v[210:211] op_sel_hi:[1,0]
	v_lshlrev_b64 v[240:241], 12, v[208:209]
	v_pk_mul_f32 v[226:227], v[152:153], v[210:211] op_sel_hi:[1,0]
	v_pk_mul_f32 v[228:229], v[150:151], v[210:211] op_sel_hi:[1,0]
	v_cvt_pk_bf16_f32 v208, v226, v227
	v_cvt_pk_bf16_f32 v209, v212, v213
	v_lshl_add_u64 v[212:213], s[26:27], 0, v[240:241]
	v_pk_mul_f32 v[230:231], v[148:149], v[210:211] op_sel_hi:[1,0]
	v_pk_mul_f32 v[232:233], v[106:107], v[210:211] op_sel_hi:[1,0]
	v_pk_mul_f32 v[234:235], v[104:105], v[210:211] op_sel_hi:[1,0]
	v_pk_mul_f32 v[236:237], v[102:103], v[210:211] op_sel_hi:[1,0]
	v_pk_mul_f32 v[238:239], v[100:101], v[210:211] op_sel_hi:[1,0]
	v_cvt_pk_bf16_f32 v210, v230, v231
	v_cvt_pk_bf16_f32 v211, v228, v229
	v_lshl_add_u64 v[212:213], v[212:213], 0, v[2:3]
	global_store_dwordx4 v[212:213], v[208:211], off sc1
	s_nop 1
	v_cvt_pk_bf16_f32 v208, v234, v235
	v_cvt_pk_bf16_f32 v209, v232, v233
	v_cvt_pk_bf16_f32 v210, v238, v239
	v_cvt_pk_bf16_f32 v211, v236, v237
	global_store_dwordx4 v[212:213], v[208:211], off offset:256 sc1
; __device__ __forceinline__ unsigned cvt_pk_bf16(float lo, float hi) { unsigned r; asm volatile("v_cvt_pk_bf16_f32 %0, %1, %2" : "=v"(r) : "v"(lo), "v"(hi)); return r; }
;     template <class Tp> __device__ __forceinline__ Tp* w(size_t off) const { return (Tp*)(ws + off); }
;     __device__ __forceinline__ void operator()(const f32x4 (&acc)[2][2][4][2], const Unit& u, int wr, int wc, int fr, int fq) const {
;     ...
;             for (int m = 0; m < 4; ++m) { const int p = row0 + ai * HALF + m * 16;
;                 if (p < lim) { const float w = wrow[lb + p]; bf16_t* rowp = Y2 + (size_t)tsi[lb + p] * 2048 + col0;
; #pragma unroll
;                     for (int bj = 0; bj < 2; ++bj) { const f32x4 v0 = acc[ai][bj][m][0] * w, v1 = acc[ai][bj][m][1] * w;
;                         u32x4 o; o.x = cvt_pk_bf16(v0[0], v0[1]); o.y = cvt_pk_bf16(v0[2], v0[3]); o.z = cvt_pk_bf16(v1[0], v1[1]); o.w = cvt_pk_bf16(v1[2], v1[3]);
;                         *(u32x4*)(rowp + bj * HALF) = o; } } }
.LBB0_1334:
	s_or_b64 exec, exec, s[10:11]
	v_add_u32_e32 v3, 0x80, v203
	v_cmp_lt_i32_e32 vcc, v3, v201
	s_and_saveexec_b64 s[10:11], vcc
	s_cbranch_execz .LBB0_1336
	v_mov_b32_e32 v208, v124
	v_mov_b32_e32 v210, v140
	v_mov_b32_e32 v3, v1
	v_ashrrev_i32_e32 v209, 31, v208
	v_pk_mul_f32 v[212:213], v[98:99], v[210:211] op_sel_hi:[1,0]
	v_lshlrev_b64 v[240:241], 12, v[208:209]
	v_pk_mul_f32 v[226:227], v[96:97], v[210:211] op_sel_hi:[1,0]
	v_pk_mul_f32 v[228:229], v[94:95], v[210:211] op_sel_hi:[1,0]
	v_cvt_pk_bf16_f32 v208, v226, v227
	v_cvt_pk_bf16_f32 v209, v212, v213
	v_lshl_add_u64 v[212:213], s[26:27], 0, v[240:241]
	v_pk_mul_f32 v[230:231], v[92:93], v[210:211] op_sel_hi:[1,0]
	v_pk_mul_f32 v[232:233], v[66:67], v[210:211] op_sel_hi:[1,0]
	v_pk_mul_f32 v[234:235], v[64:65], v[210:211] op_sel_hi:[1,0]
	v_pk_mul_f32 v[236:237], v[62:63], v[210:211] op_sel_hi:[1,0]
	v_pk_mul_f32 v[238:239], v[60:61], v[210:211] op_sel_hi:[1,0]
	v_cvt_pk_bf16_f32 v210, v230, v231
	v_cvt_pk_bf16_f32 v211, v228, v229
	v_lshl_add_u64 v[212:213], v[212:213], 0, v[2:3]
	global_store_dwordx4 v[212:213], v[208:211], off sc1
	s_nop 1
	v_cvt_pk_bf16_f32 v208, v234, v235
	v_cvt_pk_bf16_f32 v209, v232, v233
	v_cvt_pk_bf16_f32 v210, v238, v239
	v_cvt_pk_bf16_f32 v211, v236, v237
	global_store_dwordx4 v[212:213], v[208:211], off offset:256 sc1
.LBB0_1336:
	s_or_b64 exec, exec, s[10:11]
	v_add_u32_e32 v3, 0x90, v203
	v_cmp_lt_i32_e32 vcc, v3, v201
	s_and_saveexec_b64 s[10:11], vcc
	s_cbranch_execz .LBB0_1338
	v_mov_b32_e32 v208, v125
	v_mov_b32_e32 v210, v141
	v_mov_b32_e32 v3, v1
	v_ashrrev_i32_e32 v209, 31, v208
	v_pk_mul_f32 v[212:213], v[90:91], v[210:211] op_sel_hi:[1,0]
	v_lshlrev_b64 v[240:241], 12, v[208:209]
	v_pk_mul_f32 v[226:227], v[88:89], v[210:211] op_sel_hi:[1,0]
	v_pk_mul_f32 v[228:229], v[86:87], v[210:211] op_sel_hi:[1,0]
	v_cvt_pk_bf16_f32 v208, v226, v227
	v_cvt_pk_bf16_f32 v209, v212, v213
	v_lshl_add_u64 v[212:213], s[26:27], 0, v[240:241]
	v_pk_mul_f32 v[230:231], v[84:85], v[210:211] op_sel_hi:[1,0]
	v_pk_mul_f32 v[232:233], v[54:55], v[210:211] op_sel_hi:[1,0]
	v_pk_mul_f32 v[234:235], v[52:53], v[210:211] op_sel_hi:[1,0]
	v_pk_mul_f32 v[236:237], v[50:51], v[210:211] op_sel_hi:[1,0]
	v_pk_mul_f32 v[238:239], v[48:49], v[210:211] op_sel_hi:[1,0]
	v_cvt_pk_bf16_f32 v210, v230, v231
	v_cvt_pk_bf16_f32 v211, v228, v229
	v_lshl_add_u64 v[212:213], v[212:213], 0, v[2:3]
	global_store_dwordx4 v[212:213], v[208:211], off sc1
	s_nop 1
	v_cvt_pk_bf16_f32 v208, v234, v235
	v_cvt_pk_bf16_f32 v209, v232, v233
	v_cvt_pk_bf16_f32 v210, v238, v239
	v_cvt_pk_bf16_f32 v211, v236, v237
	global_store_dwordx4 v[212:213], v[208:211], off offset:256 sc1
.LBB0_1338:
	s_or_b64 exec, exec, s[10:11]
	v_add_u32_e32 v3, 0xa0, v203
	v_cmp_lt_i32_e32 vcc, v3, v201
	s_and_saveexec_b64 s[10:11], vcc
	s_cbranch_execz .LBB0_1340
	v_mov_b32_e32 v208, v126
	v_mov_b32_e32 v210, v142
	v_mov_b32_e32 v3, v1
	v_ashrrev_i32_e32 v209, 31, v208
	v_pk_mul_f32 v[212:213], v[82:83], v[210:211] op_sel_hi:[1,0]
	v_lshlrev_b64 v[240:241], 12, v[208:209]
	v_pk_mul_f32 v[226:227], v[80:81], v[210:211] op_sel_hi:[1,0]
	v_pk_mul_f32 v[228:229], v[78:79], v[210:211] op_sel_hi:[1,0]
	v_cvt_pk_bf16_f32 v208, v226, v227
	v_cvt_pk_bf16_f32 v209, v212, v213
	v_lshl_add_u64 v[212:213], s[26:27], 0, v[240:241]
	v_pk_mul_f32 v[230:231], v[76:77], v[210:211] op_sel_hi:[1,0]
	v_pk_mul_f32 v[232:233], v[46:47], v[210:211] op_sel_hi:[1,0]
	v_pk_mul_f32 v[234:235], v[44:45], v[210:211] op_sel_hi:[1,0]
	v_pk_mul_f32 v[236:237], v[42:43], v[210:211] op_sel_hi:[1,0]
	v_pk_mul_f32 v[238:239], v[40:41], v[210:211] op_sel_hi:[1,0]
	v_cvt_pk_bf16_f32 v210, v230, v231
	v_cvt_pk_bf16_f32 v211, v228, v229
	v_lshl_add_u64 v[212:213], v[212:213], 0, v[2:3]
	global_store_dwordx4 v[212:213], v[208:211], off sc1
	s_nop 1
	v_cvt_pk_bf16_f32 v208, v234, v235
	v_cvt_pk_bf16_f32 v209, v232, v233
	v_cvt_pk_bf16_f32 v210, v238, v239
	v_cvt_pk_bf16_f32 v211, v236, v237
	global_store_dwordx4 v[212:213], v[208:211], off offset:256 sc1
.LBB0_1340:
	s_or_b64 exec, exec, s[10:11]
	v_add_u32_e32 v3, 0xb0, v203
	v_cmp_lt_i32_e32 vcc, v3, v201
	s_and_saveexec_b64 s[10:11], vcc
	s_cbranch_execz .LBB0_1342
	v_mov_b32_e32 v208, v127
	v_mov_b32_e32 v210, v143
	v_mov_b32_e32 v3, v1
	v_ashrrev_i32_e32 v209, 31, v208
	v_pk_mul_f32 v[212:213], v[74:75], v[210:211] op_sel_hi:[1,0]
	v_lshlrev_b64 v[240:241], 12, v[208:209]
	v_pk_mul_f32 v[226:227], v[72:73], v[210:211] op_sel_hi:[1,0]
	v_pk_mul_f32 v[228:229], v[70:71], v[210:211] op_sel_hi:[1,0]
	v_cvt_pk_bf16_f32 v208, v226, v227
	v_cvt_pk_bf16_f32 v209, v212, v213
	v_lshl_add_u64 v[212:213], s[26:27], 0, v[240:241]
	v_pk_mul_f32 v[230:231], v[68:69], v[210:211] op_sel_hi:[1,0]
	v_pk_mul_f32 v[232:233], v[38:39], v[210:211] op_sel_hi:[1,0]
	v_pk_mul_f32 v[234:235], v[36:37], v[210:211] op_sel_hi:[1,0]
	v_pk_mul_f32 v[236:237], v[34:35], v[210:211] op_sel_hi:[1,0]
	v_pk_mul_f32 v[238:239], v[32:33], v[210:211] op_sel_hi:[1,0]
	v_cvt_pk_bf16_f32 v210, v230, v231
	v_cvt_pk_bf16_f32 v211, v228, v229
	v_lshl_add_u64 v[2:3], v[212:213], 0, v[2:3]
	global_store_dwordx4 v[2:3], v[208:211], off sc1
	s_nop 1
	v_cvt_pk_bf16_f32 v208, v234, v235
	v_cvt_pk_bf16_f32 v209, v232, v233
	v_cvt_pk_bf16_f32 v210, v238, v239
	v_cvt_pk_bf16_f32 v211, v236, v237
	global_store_dwordx4 v[2:3], v[208:211], off offset:256 sc1
